# attention: even-step row loads issued on every iteration (last one re-reads current rows), odd-step compute waits count them as outstanding (vmcnt +16), vmcnt(0) at loop exit; on top of v14
# baseline (speedup 1.0000x reference)
.LBB0_738:
	v_mul_f32_e32 v187, 0xbe38aa3b, v202
	v_fmamk_f32 v0, v182, 0x3e38aa3b, v187
	v_exp_f32_e32 v0, v0
	v_fmamk_f32 v182, v183, 0x3e38aa3b, v187
	v_exp_f32_e32 v186, v182
	v_fmamk_f32 v182, v184, 0x3e38aa3b, v187
	v_exp_f32_e32 v184, v182
	v_fmamk_f32 v182, v185, 0x3e38aa3b, v187
	v_exp_f32_e32 v185, v182
	v_fmamk_f32 v178, v178, 0x3e38aa3b, v187
	v_add_f32_e32 v153, 0, v0
	v_exp_f32_e32 v178, v178
	v_fmamk_f32 v179, v179, 0x3e38aa3b, v187
	v_add_f32_e32 v153, v186, v153
	v_exp_f32_e32 v179, v179
	v_fmamk_f32 v180, v180, 0x3e38aa3b, v187
	v_add_f32_e32 v153, v184, v153
	v_exp_f32_e32 v180, v180
	v_fmamk_f32 v181, v181, 0x3e38aa3b, v187
	v_add_f32_e32 v153, v185, v153
	v_exp_f32_e32 v181, v181
	v_fmamk_f32 v174, v174, 0x3e38aa3b, v187
	v_add_f32_e32 v153, v178, v153
	v_exp_f32_e32 v188, v174
	v_fmamk_f32 v174, v175, 0x3e38aa3b, v187
	v_add_f32_e32 v153, v179, v153
	v_exp_f32_e32 v189, v174
	v_fmamk_f32 v174, v176, 0x3e38aa3b, v187
	v_add_f32_e32 v153, v180, v153
	v_exp_f32_e32 v190, v174
	v_fmamk_f32 v174, v177, 0x3e38aa3b, v187
	v_add_f32_e32 v153, v181, v153
	v_exp_f32_e32 v191, v174
	v_fmamk_f32 v170, v170, 0x3e38aa3b, v187
	v_add_f32_e32 v153, v188, v153
	v_exp_f32_e32 v192, v170
	v_fmamk_f32 v170, v171, 0x3e38aa3b, v187
	v_add_f32_e32 v153, v189, v153
	v_exp_f32_e32 v193, v170
	v_fmamk_f32 v170, v172, 0x3e38aa3b, v187
	v_add_f32_e32 v153, v190, v153
	v_exp_f32_e32 v194, v170
	v_fmamk_f32 v170, v173, 0x3e38aa3b, v187
	v_add_f32_e32 v153, v191, v153
	v_exp_f32_e32 v195, v170
	v_add_f32_e32 v153, v192, v153
	v_add_f32_e32 v153, v193, v153
	v_add_f32_e32 v153, v194, v153
	v_add_f32_e32 v153, v195, v153
	v_mov_b32_e32 v170, v153
	s_nop 1
	v_permlane16_swap_b32_e32 v153, v170
	v_add_f32_e32 v182, v153, v170
	v_mov_b32_e32 v183, v182
	s_waitcnt vmcnt(23)
	ds_write_b128 v235, v[46:49]
	s_waitcnt vmcnt(22)
	ds_write_b128 v235, v[50:53] offset:1024
	s_waitcnt vmcnt(21)
	ds_write_b128 v235, v[62:65] offset:2048
	s_waitcnt vmcnt(20)
	ds_write_b128 v235, v[66:69] offset:3072
	v_cvt_pk_bf16_f32 v170, v0, v186
	v_cvt_pk_bf16_f32 v171, v184, v185
	v_cvt_pk_bf16_f32 v172, v178, v179
	v_cvt_pk_bf16_f32 v173, v180, v181
	ds_read_b64_tr_b16 v[174:175], v236
	ds_read_b64_tr_b16 v[176:177], v237
	s_waitcnt lgkmcnt(0)
	v_mfma_f32_16x16x32_bf16 v[166:169], v[174:177], v[170:173], v[166:169]
	ds_read_b64_tr_b16 v[174:175], v238
	ds_read_b64_tr_b16 v[176:177], v239
	v_permlane32_swap_b32_e32 v182, v183
	s_waitcnt lgkmcnt(0)
	v_mfma_f32_16x16x32_bf16 v[162:165], v[174:177], v[170:173], v[162:165]
	ds_read_b64_tr_b16 v[174:175], v240
	ds_read_b64_tr_b16 v[176:177], v241
	s_waitcnt lgkmcnt(0)
	v_mfma_f32_16x16x32_bf16 v[174:177], v[174:177], v[170:173], v[158:161]
	s_nop 2
	ds_read_b64_tr_b16 v[158:159], v242
	ds_read_b64_tr_b16 v[160:161], v243
	s_waitcnt vmcnt(19)
	ds_write_b128 v235, v[70:73]
	s_waitcnt vmcnt(18)
	ds_write_b128 v235, v[74:77] offset:1024
	s_waitcnt vmcnt(17)
	ds_write_b128 v235, v[78:81] offset:2048
	s_waitcnt vmcnt(16)
	ds_write_b128 v235, v[82:85] offset:3072
	s_waitcnt lgkmcnt(4)
	v_mfma_f32_16x16x32_bf16 v[170:173], v[158:161], v[170:173], v[154:157]
	v_cvt_pk_bf16_f32 v178, v188, v189
	v_cvt_pk_bf16_f32 v179, v190, v191
	v_cvt_pk_bf16_f32 v180, v192, v193
	v_cvt_pk_bf16_f32 v181, v194, v195
	s_nop 2
	ds_read_b64_tr_b16 v[154:155], v236
	ds_read_b64_tr_b16 v[156:157], v237
	ds_read_b64_tr_b16 v[158:159], v238
	ds_read_b64_tr_b16 v[160:161], v239
	s_waitcnt lgkmcnt(2)
	v_mfma_f32_16x16x32_bf16 v[154:157], v[154:157], v[178:181], v[166:169]
	s_waitcnt lgkmcnt(0)
	v_mfma_f32_16x16x32_bf16 v[158:161], v[158:161], v[178:181], v[162:165]
	s_nop 2
	ds_read_b64_tr_b16 v[162:163], v240
	ds_read_b64_tr_b16 v[164:165], v241
	ds_read_b64_tr_b16 v[166:167], v242
	ds_read_b64_tr_b16 v[168:169], v243
	s_waitcnt lgkmcnt(2)
	v_mfma_f32_16x16x32_bf16 v[162:165], v[162:165], v[178:181], v[174:177]
	s_waitcnt lgkmcnt(0)
	v_mfma_f32_16x16x32_bf16 v[166:169], v[166:169], v[178:181], v[170:173]
	s_cmp_ge_u32 s47, s18
	s_cselect_b64 s[36:37], -1, 0
	s_and_b64 vcc, exec, s[36:37]
	s_cbranch_vccz .Lattn_realA_a
	s_add_i32 s12, s47, -2
	s_lshr_b32 s13, s12, 2
	s_add_i32 s13, s13, s44
	s_lshl_b32 s13, s13, 9
	s_and_b32 s12, s12, 2
	s_lshl_b32 s12, s12, 7
	s_add_i32 s12, s12, s13
	s_branch .Lattn_blkA_a
.Lattn_realA_a:
	s_lshr_b32 s35, s47, 2
	s_and_b32 s34, s47, 2
	s_add_i32 s35, s35, s44
	s_cmp_lg_u32 s34, 0
	s_cbranch_scc1 .LBB0_745
	s_add_u32 s12, s45, s35
	s_addc_u32 s13, s46, 0
	v_mov_b32_e32 v0, 0x1200
	v_mov_b32_e32 v56, v1
	v_mov_b32_e32 v57, v1
	s_mul_i32 s56, s13, 0x1200
	v_mad_u64_u32 v[14:15], s[12:13], s12, v0, v[214:215]
	v_mov_b32_e32 v54, v1
	v_mov_b32_e32 v55, v1
	v_mov_b64_e32 v[60:61], v[56:57]
	v_add_u32_e32 v15, s56, v15
	v_mov_b64_e32 v[58:59], v[54:55]
	s_and_saveexec_b64 s[12:13], s[28:29]
	s_cbranch_execz .LBB0_742
	global_load_dwordx4 v[58:61], v[14:15], off offset:512

.Lattn_blkA_a:
	v_lshl_add_u32 v70, v233, 1, s12
	ds_read_u16 v46, v70 offset:32768
	ds_read_u16 v50, v70 offset:32784
	ds_read_u16 v62, v70 offset:32800
	ds_read_u16 v66, v70 offset:32816
	ds_read_u16 v71, v70 offset:32832
	ds_read_u16 v74, v70 offset:32848
	ds_read_u16 v78, v70 offset:32864
	ds_read_u16 v82, v70 offset:32880
	s_waitcnt lgkmcnt(7)
	v_lshlrev_b32_e32 v0, 9, v46
	v_lshl_add_u64 v[46:47], v[212:213], 0, v[0:1]
	global_load_dwordx4 v[14:17], v[46:47], off
	s_waitcnt lgkmcnt(6)
	v_lshlrev_b32_e32 v0, 9, v50
	v_lshl_add_u64 v[50:51], v[212:213], 0, v[0:1]
	global_load_dwordx4 v[18:21], v[50:51], off
	s_waitcnt lgkmcnt(5)
	v_lshlrev_b32_e32 v0, 9, v62
	v_lshl_add_u64 v[62:63], v[212:213], 0, v[0:1]
	global_load_dwordx4 v[22:25], v[62:63], off
	s_waitcnt lgkmcnt(4)
	v_lshlrev_b32_e32 v0, 9, v66
	v_lshl_add_u64 v[66:67], v[212:213], 0, v[0:1]
	global_load_dwordx4 v[26:29], v[66:67], off
	s_waitcnt lgkmcnt(3)
	v_lshlrev_b32_e32 v0, 9, v71
	v_lshl_add_u64 v[70:71], v[212:213], 0, v[0:1]
	global_load_dwordx4 v[30:33], v[70:71], off
	s_waitcnt lgkmcnt(2)
	v_lshlrev_b32_e32 v0, 9, v74
	v_lshl_add_u64 v[74:75], v[212:213], 0, v[0:1]
	global_load_dwordx4 v[34:37], v[74:75], off
	s_waitcnt lgkmcnt(1)
	v_lshlrev_b32_e32 v0, 9, v78
	v_lshl_add_u64 v[78:79], v[212:213], 0, v[0:1]
	global_load_dwordx4 v[38:41], v[78:79], off
	s_waitcnt lgkmcnt(0)
	v_lshlrev_b32_e32 v0, 9, v82
	v_lshl_add_u64 v[82:83], v[212:213], 0, v[0:1]
	global_load_dwordx4 v[42:45], v[82:83], off
	global_load_dwordx4 v[46:49], v[46:47], off offset:128
	s_nop 0
	global_load_dwordx4 v[50:53], v[50:51], off offset:128
	s_nop 0
	global_load_dwordx4 v[62:65], v[62:63], off offset:128
	s_nop 0
	global_load_dwordx4 v[66:69], v[66:67], off offset:128
	s_nop 0
	global_load_dwordx4 v[70:73], v[70:71], off offset:128
	s_nop 0
	global_load_dwordx4 v[74:77], v[74:75], off offset:128
	s_nop 0
	global_load_dwordx4 v[78:81], v[78:79], off offset:128
	s_nop 0
	global_load_dwordx4 v[82:85], v[82:83], off offset:128

.LBB0_760:
	s_waitcnt vmcnt(24)
	ds_write_b128 v196, v[138:141]
	ds_write_b128 v197, v[142:145] offset:1024
	ds_write_b128 v196, v[146:149] offset:2048
	ds_write_b128 v197, v[134:137] offset:3072
	ds_read_b128 v[138:141], v198
	ds_read_b128 v[142:145], v199
	ds_read_b128 v[146:149], v198 offset:2048
	ds_read_b128 v[134:137], v199 offset:2048
	ds_write_b128 v196, v[130:133]
	ds_write_b128 v197, v[126:129] offset:1024
	ds_write_b128 v196, v[122:125] offset:2048
	ds_write_b128 v197, v[118:121] offset:3072
	ds_read_b128 v[130:133], v198
	ds_read_b128 v[126:129], v199
	ds_read_b128 v[122:125], v198 offset:2048
	ds_read_b128 v[118:121], v199 offset:2048
	s_waitcnt lgkmcnt(0)
	s_waitcnt vmcnt(31)
	v_mfma_f32_16x16x32_bf16 v[138:141], v[138:141], v[6:9], v[150:153]
	v_add_f32_e32 v0, v182, v183
	s_mov_b32 s12, 0x40c00000
	s_waitcnt vmcnt(27)
	v_mfma_f32_16x16x32_bf16 v[130:133], v[130:133], v[6:9], v[174:177]
	s_waitcnt vmcnt(25) lgkmcnt(0)
	v_mfma_f32_16x16x32_bf16 v[122:125], v[122:125], v[6:9], v[178:181]
	v_mfma_f32_16x16x32_bf16 v[138:141], v[142:145], v[10:13], v[138:141]
	v_add_f32_e32 v142, v244, v0
	v_mfma_f32_16x16x32_bf16 v[144:147], v[146:149], v[6:9], v[170:173]
	v_mfma_f32_16x16x32_bf16 v[126:129], v[126:129], v[10:13], v[130:133]
	s_nop 4
	v_max_f32_e32 v0, v141, v141
	v_max_f32_e32 v143, v140, v140
	v_max_f32_e32 v0, v143, v0
	s_waitcnt vmcnt(24)
	v_mfma_f32_16x16x32_bf16 v[118:121], v[118:121], v[10:13], v[122:125]
	v_max3_f32 v0, v138, v139, v0
	v_max_f32_e32 v130, v127, v127
	v_max_f32_e32 v131, v126, v126
	v_mfma_f32_16x16x32_bf16 v[134:137], v[134:137], v[10:13], v[144:147]
	v_max_f32_e32 v130, v131, v130
	s_nop 2
	v_max_f32_e32 v122, v121, v121
	v_max_f32_e32 v123, v120, v120
	v_max_f32_e32 v131, v129, v129
	v_max_f32_e32 v132, v128, v128
	v_max_f32_e32 v143, v137, v137
	v_max_f32_e32 v144, v136, v136
	v_max_f32_e32 v122, v123, v122
	v_max_f32_e32 v143, v144, v143
	v_max_f32_e32 v131, v132, v131
	v_max3_f32 v122, v118, v119, v122
	v_max3_f32 v143, v134, v135, v143
	v_max3_f32 v122, v130, v131, v122
	v_max3_f32 v0, v0, v143, v122
	v_mov_b32_e32 v122, v0
	s_nop 1
	v_permlane16_swap_b32_e32 v0, v122
	v_max_f32_e32 v122, v122, v122
	v_max_f32_e32 v0, v0, v0
	v_max_f32_e32 v0, v0, v122
	v_mov_b32_e32 v122, v0
	s_nop 1
	v_permlane32_swap_b32_e32 v0, v122
	v_max_f32_e32 v122, v122, v122
	v_max_f32_e32 v0, v0, v0
	v_max_f32_e32 v0, v0, v122
	v_sub_f32_e32 v122, v0, v202
	v_mul_f32_e32 v122, 0x3e38aa3b, v122
	v_cmp_lt_f32_e32 vcc, s12, v122
	s_cbranch_vccz .LBB0_762
	v_max_f32_e32 v0, v0, v0
	v_max_f32_e32 v122, v202, v202
	v_max_f32_e32 v143, v122, v0
	v_sub_f32_e32 v0, v202, v143
	v_mul_f32_e32 v0, 0x3e38aa3b, v0
	v_exp_f32_e32 v202, v0
	s_nop 0
	v_pk_mul_f32 v[186:187], v[142:143], v[202:203]
	v_pk_mul_f32 v[156:157], v[156:157], v[202:203] op_sel_hi:[1,0]
	v_pk_mul_f32 v[154:155], v[154:155], v[202:203] op_sel_hi:[1,0]
	v_pk_mul_f32 v[160:161], v[160:161], v[202:203] op_sel_hi:[1,0]
	v_pk_mul_f32 v[158:159], v[158:159], v[202:203] op_sel_hi:[1,0]
	v_pk_mul_f32 v[164:165], v[164:165], v[202:203] op_sel_hi:[1,0]
	v_pk_mul_f32 v[162:163], v[162:163], v[202:203] op_sel_hi:[1,0]
	v_pk_mul_f32 v[168:169], v[168:169], v[202:203] op_sel_hi:[1,0]
	v_pk_mul_f32 v[166:167], v[166:167], v[202:203] op_sel_hi:[1,0]
	v_mov_b32_e32 v202, v143
	v_mov_b32_e32 v142, v186

.LBB0_766:
	s_waitcnt vmcnt(0)
	s_waitcnt lgkmcnt(0)
	s_barrier
	s_mov_b64 s[0:1], 0
